# XCD leader waits only for its wbl2 before the TOP atomic; its L1 invalidate overlaps the TOP round trip (on top of early-invalidate + release broadcast)
# baseline (speedup 1.0000x reference)
; __device__ __forceinline__ unsigned xb_add(unsigned* p, unsigned v) { return __hip_atomic_fetch_add(p, v, __ATOMIC_RELAXED, __HIP_MEMORY_SCOPE_AGENT); }
; __device__ __forceinline__ void xcd_barrier(const XcdBarrier& b) {
;     ...
;         if (old + 1u == (gen + 1u) * nloc) {
;             __builtin_amdgcn_fence(__ATOMIC_RELEASE, "agent");
;             asm volatile("s_waitcnt vmcnt(0)" ::: "memory");
;             const unsigned og = xb_add(&bar[XB_TOP], 1u);
;             const unsigned tg = og / nx;
;             if (og + 1u == (tg + 1u) * nx) xb_add(&bar[XB_TOPGEN], 1u);
.LBB0_79:
	s_andn2_saveexec_b64 s[4:5], s[4:5]
	s_cbranch_execz .LBB0_97
	s_mov_b64 s[4:5], exec
	buffer_wbl2 sc1
	s_waitcnt lgkmcnt(0)
	s_waitcnt vmcnt(0)
	buffer_inv sc1
	v_mbcnt_lo_u32_b32 v2, s4, 0
	v_mbcnt_hi_u32_b32 v2, s5, v2
	v_cmp_eq_u32_e32 vcc, 0, v2
	s_and_saveexec_b64 s[6:7], vcc
	s_cbranch_execz .LBB0_82
	s_bcnt1_i32_b64 s4, s[4:5]
	v_mov_b32_e32 v3, 0x7000
	v_mov_b32_e32 v4, s4
	global_atomic_add v3, v3, v4, s[94:95] offset:1024 sc0

; __device__ __forceinline__ unsigned xb_add(unsigned* p, unsigned v) { return __hip_atomic_fetch_add(p, v, __ATOMIC_RELAXED, __HIP_MEMORY_SCOPE_AGENT); }
; __device__ __forceinline__ void xcd_barrier(const XcdBarrier& b) {
;     ...
;         if (old + 1u == (gen + 1u) * nloc) {
;             __builtin_amdgcn_fence(__ATOMIC_RELEASE, "agent");
;             asm volatile("s_waitcnt vmcnt(0)" ::: "memory");
;             const unsigned og = xb_add(&bar[XB_TOP], 1u);
;             const unsigned tg = og / nx;
;             if (og + 1u == (tg + 1u) * nx) xb_add(&bar[XB_TOPGEN], 1u);
.LBB0_240:
	s_andn2_saveexec_b64 s[4:5], s[4:5]
	s_cbranch_execz .LBB0_258
	s_mov_b64 s[4:5], exec
	buffer_wbl2 sc1
	s_waitcnt lgkmcnt(0)
	s_waitcnt vmcnt(0)
	buffer_inv sc1
	v_mbcnt_lo_u32_b32 v3, s4, 0
	v_mbcnt_hi_u32_b32 v3, s5, v3
	v_cmp_eq_u32_e32 vcc, 0, v3
	s_and_saveexec_b64 s[6:7], vcc
	s_cbranch_execz .LBB0_243
	s_bcnt1_i32_b64 s4, s[4:5]
	v_mov_b32_e32 v4, 0x7000
	v_mov_b32_e32 v5, s4
	global_atomic_add v4, v4, v5, s[94:95] offset:1024 sc0

; __device__ __forceinline__ unsigned xb_add(unsigned* p, unsigned v) { return __hip_atomic_fetch_add(p, v, __ATOMIC_RELAXED, __HIP_MEMORY_SCOPE_AGENT); }
; __device__ __forceinline__ void xcd_barrier(const XcdBarrier& b) {
;     ...
;         if (old + 1u == (gen + 1u) * nloc) {
;             __builtin_amdgcn_fence(__ATOMIC_RELEASE, "agent");
;             asm volatile("s_waitcnt vmcnt(0)" ::: "memory");
;             const unsigned og = xb_add(&bar[XB_TOP], 1u);
;             const unsigned tg = og / nx;
;             if (og + 1u == (tg + 1u) * nx) xb_add(&bar[XB_TOPGEN], 1u);
.LBB0_2309:
	s_andn2_saveexec_b64 s[12:13], s[42:43]
	s_cbranch_execz .LBB0_2203
	s_mov_b64 s[42:43], exec
	buffer_wbl2 sc1
	s_waitcnt lgkmcnt(0)
	s_waitcnt vmcnt(0)
	buffer_inv sc1
	v_mbcnt_lo_u32_b32 v3, s42, 0
	v_mbcnt_hi_u32_b32 v3, s43, v3
	v_cmp_eq_u32_e32 vcc, 0, v3
	s_and_saveexec_b64 s[46:47], vcc
	s_cbranch_execz .LBB0_2312
	s_bcnt1_i32_b64 s2, s[42:43]
	v_readlane_b32 s12, v255, 9
	v_mov_b32_e32 v4, s2
	v_readlane_b32 s13, v255, 10
	s_nop 4
	global_atomic_add v4, v133, v4, s[12:13] sc0

; __device__ __forceinline__ unsigned xb_add(unsigned* p, unsigned v) { return __hip_atomic_fetch_add(p, v, __ATOMIC_RELAXED, __HIP_MEMORY_SCOPE_AGENT); }
; __device__ __forceinline__ void xcd_barrier(const XcdBarrier& b) {
;     ...
;         if (old + 1u == (gen + 1u) * nloc) {
;             __builtin_amdgcn_fence(__ATOMIC_RELEASE, "agent");
;             asm volatile("s_waitcnt vmcnt(0)" ::: "memory");
;             const unsigned og = xb_add(&bar[XB_TOP], 1u);
;             const unsigned tg = og / nx;
;             if (og + 1u == (tg + 1u) * nx) xb_add(&bar[XB_TOPGEN], 1u);
.LBB0_4572:
	s_andn2_saveexec_b64 s[0:1], s[22:23]
	s_cbranch_execz .LBB0_4466
	s_mov_b64 s[22:23], exec
	buffer_wbl2 sc1
	s_waitcnt lgkmcnt(0)
	s_waitcnt vmcnt(0)
	buffer_inv sc1
	v_mbcnt_lo_u32_b32 v3, s22, 0
	v_mbcnt_hi_u32_b32 v3, s23, v3
	v_cmp_eq_u32_e32 vcc, 0, v3
	s_and_saveexec_b64 s[38:39], vcc
	s_cbranch_execz .LBB0_4575
	s_bcnt1_i32_b64 s0, s[22:23]
	v_mov_b32_e32 v4, s0
	v_readlane_b32 s0, v254, 57
	v_readlane_b32 s1, v254, 58
	s_nop 4
	global_atomic_add v4, v133, v4, s[0:1] sc0
